# P8: wave group 0 alignment barrier deferred from after the K-loop to the head of the epilogue (unit scheduling overlaps group 1 last MFMA interval)
# baseline (speedup 1.0000x reference)
; #define LAS __attribute__((address_space(3)))
;     __device__ __forceinline__ bool next(int i, pg8::Unit& u) const { const int L = i * G + c; if (L >= nM * 4) return false; int pm, pn; pg8::tile_remap<4>(L, nM, pm, pn); if (rev) pm = nM - 1 - pm; u.pm = pm; u.pn = pn; u.aux = 0; u.skip = 0; return true; }
;     __device__ __forceinline__ bool next(int i, pg8::Unit& u) const { const int L = first + i * stride; if (i >= nmine || L >= 512) return false; u.pm = L & 3; u.pn = (L >> 2) & 3; u.aux = L >> 4; u.skip = 0; return true; }
;     __device__ __forceinline__ bool next(int i, pg8::Unit& u) const { if (!TW) { const bool r = Base::next(i, u); u.skip = 0; return r; } const bool r = Base::next(i >> 1, u); u.skip = !(i & 1); return r; }
;     const int nwg = nM * NN; int wgid = L;
;     { const int q = nwg >> 3, r = nwg & 7, xcd = wgid & 7, off = wgid >> 3; wgid = (xcd < r ? xcd * (q + 1) : r * (q + 1) + (xcd - r) * q) + off; }
;     constexpr int nig = WGM * NN; const int gid = wgid / nig, idx = wgid - gid * nig, fm = gid * WGM, left = nM - fm;
;     if (left >= WGM) { pm = fm + (idx % WGM); pn = idx / WGM; } else { pm = fm + (idx % left); pn = idx / left; }
; }
;     __device__ __forceinline__ bool next(int i, pg8::Unit& u) const {
;         const int L = i * G + c; if (L >= NT * NN) return false; pg8::tile_remap<NN>(L, NT, u.pm, u.pn);
;         if (!GATH) u.pm = NT - 1 - u.pm;
;         u.aux = __builtin_amdgcn_readfirstlane((int)((const LAS unsigned char*)tpre + 11264)[u.pm]); u.skip = 0; return true; }
.LBB0_961:
.LBB0_963:
	v_cndmask_b32_e64 v2, 0, 1, s[10:11]
	v_cmp_ne_u32_e64 s[2:3], 1, v2
	s_andn2_b64 vcc, exec, s[10:11]
	s_cbranch_vccnz .LBB0_968
	s_add_i32 s10, s43, 2
	s_mul_i32 s10, s10, s92
	s_add_i32 s10, s10, s33
	s_cmp_lt_i32 s10, s19
	s_cselect_b64 s[24:25], -1, 0
	s_cmp_ge_i32 s10, s19
	s_cbranch_scc1 .LBB0_966
	s_ashr_i32 s11, s10, 3
	s_and_b32 s10, s10, 7
	s_mul_i32 s10, s10, s17
	s_add_i32 s10, s10, s11
	s_ashr_i32 s11, s10, 31
	s_lshr_b32 s11, s11, 26
	s_add_i32 s11, s10, s11
	s_ashr_i32 s11, s11, 6
	s_lshl_b32 s23, s11, 3
	s_sub_i32 s26, s17, s23
	s_min_i32 s26, s26, 8
	s_abs_i32 s27, s26
	v_cvt_f32_u32_e32 v2, s27
	s_sub_i32 s29, 0, s27
	s_lshl_b32 s11, s11, 6
	s_sub_i32 s10, s10, s11
	v_rcp_iflag_f32_e32 v2, v2
	s_abs_i32 s11, s10
	s_xor_b32 s28, s10, s26
	s_ashr_i32 s28, s28, 31
	v_mul_f32_e32 v2, 0x4f7ffffe, v2
	v_cvt_u32_f32_e32 v2, v2
	s_nop 0
	v_readfirstlane_b32 s30, v2
	s_mul_i32 s29, s29, s30
	s_mul_hi_u32 s29, s30, s29
	s_add_i32 s30, s30, s29
	s_mul_hi_u32 s29, s11, s30
	s_mul_i32 s30, s29, s27
	s_sub_i32 s11, s11, s30
	s_add_i32 s31, s29, 1
	s_sub_i32 s30, s11, s27
	s_cmp_ge_u32 s11, s27
	s_cselect_b32 s29, s31, s29
	s_cselect_b32 s11, s30, s11
	s_add_i32 s30, s29, 1
	s_cmp_ge_u32 s11, s27
	s_cselect_b32 s11, s30, s29
	s_xor_b32 s11, s11, s28
	s_sub_i32 s39, s11, s28
	s_mul_i32 s11, s39, s26
	s_sub_i32 s10, s10, s11
	s_add_i32 s40, s10, s23
	s_add_i32 s10, s40, 0
	s_add_i32 s10, s10, 0x23000
	v_mov_b32_e32 v2, s10
	ds_read_u8 v2, v2
	s_waitcnt lgkmcnt(0)
	v_readfirstlane_b32 s41, v2

; __device__ __forceinline__ unsigned pk4_fp8(float a, float b, float c, float d) { int w = __builtin_amdgcn_cvt_pk_fp8_f32(a, b, 0, false); w = __builtin_amdgcn_cvt_pk_fp8_f32(c, d, w, true); return (unsigned)w; }
;     static __device__ __forceinline__ f32x2 act2(f32x2 g, f32x2 u) {
;         g.x = __builtin_amdgcn_fmed3f(g.x, -24.0f, 7.0f); g.y = __builtin_amdgcn_fmed3f(g.y, -24.0f, 7.0f);
;         u.x = __builtin_amdgcn_fmed3f(u.x, -7.0f, 7.0f); u.y = __builtin_amdgcn_fmed3f(u.y, -7.0f, 7.0f);
;         f32x2 z = g * (-1.702f * 1.4426950408889634f);
;         f32x2 d; d.x = __builtin_amdgcn_exp2f(z.x); d.y = __builtin_amdgcn_exp2f(z.y);
;         d = d + 1.0f;
;         const float r = __builtin_amdgcn_rcpf(d.x * d.y);
;         f32x2 sg; sg.x = r * d.y; sg.y = r * d.x;
;         return (u + 1.0f) * (g * sg);
;     }
;     __device__ __forceinline__ void operator()(const f32x4 (&acc)[2][2][4][2], const pg8::Unit& u, int wr, int wc, int fr, int fq) const {
;         const int e = u.aux;
;         unsigned char* Ht = ws + WS_H2 + (size_t)u.pm * TSF8;
;         const int hc = u.pn * 128 + wc * 32 + 8 * fq;
;         const f32x4 bg0 = *(const f32x4*)(bgate + e * FF + hc), bg1 = *(const f32x4*)(bgate + e * FF + hc + 4);
;         const f32x4 bu0 = *(const f32x4*)(bup + e * FF + hc), bu1 = *(const f32x4*)(bup + e * FF + hc + 4);
; #pragma unroll
;         for (int ai = 0; ai < 2; ++ai)
; #pragma unroll
;             for (int m = 0; m < 4; ++m) { const int rl = ai * 128 + wr * 64 + m * 16 + fr;
;                 const f32x4 g0 = acc[ai][0][m][0] * (1.0f / 64.0f) + bg0, g1 = acc[ai][0][m][1] * (1.0f / 64.0f) + bg1, u0 = acc[ai][1][m][0] * (1.0f / 64.0f) + bu0, u1 = acc[ai][1][m][1] * (1.0f / 64.0f) + bu1;
;                 const f32x2 h0 = act2((f32x2){g0[0], g0[1]}, (f32x2){u0[0], u0[1]}), h1 = act2((f32x2){g0[2], g0[3]}, (f32x2){u0[2], u0[3]});
;                 const f32x2 h2 = act2((f32x2){g1[0], g1[1]}, (f32x2){u1[0], u1[1]}), h3 = act2((f32x2){g1[2], g1[3]}, (f32x2){u1[2], u1[3]});
;                 *(u32x2*)(Ht + (size_t)rl * FF + hc) = (u32x2){pk4_fp8(h0.x, h0.y, h1.x, h1.y), pk4_fp8(h2.x, h2.y, h3.x, h3.y)}; }
.LBB0_968:
	s_mov_b64 s[10:11], 0
	v_mov_b32_e32 v2, v66
	v_mov_b32_e32 v3, v67
	v_mov_b32_e32 v4, v68
	v_mov_b32_e32 v5, v69
.LBB0_969:
	s_and_b64 vcc, exec, s[14:15]
	s_cbranch_vccz .Lmy_nobar0
	s_barrier
.Lmy_nobar0:
	s_ashr_i32 s23, s22, 31
	s_lshl_b64 s[22:23], s[22:23], 18
	v_mov_b32_e32 v24, v0
	s_add_u32 s22, s46, s22
	s_addc_u32 s23, s47, s23
	s_lshl_b32 s24, s62, 7
	v_lshrrev_b32_e32 v6, 1, v24
	v_and_or_b32 v6, v6, 24, s24
	s_lshl_b32 s24, s61, 10
	s_ashr_i32 s25, s24, 31
	v_or_b32_e32 v22, s45, v6
	s_lshl_b64 s[24:25], s[24:25], 2
	s_add_u32 s26, s84, s24
	v_ashrrev_i32_e32 v23, 31, v22
	s_addc_u32 s27, s85, s25
	v_lshlrev_b64 v[6:7], 2, v[22:23]
	v_lshl_add_u64 v[8:9], s[26:27], 0, v[6:7]
	s_add_u32 s24, s88, s24
	s_addc_u32 s25, s89, s25
	v_lshl_add_u64 v[6:7], s[24:25], 0, v[6:7]
	s_nop 0
	v_and_or_b32 v26, v24, 15, s44
	v_ashrrev_i32_e32 v27, 31, v26
	v_lshlrev_b64 v[32:33], 10, v[26:27]
	v_lshl_add_u64 v[24:25], s[22:23], 0, v[22:23]
	v_lshl_add_u64 v[22:23], v[24:25], 0, v[32:33]
	v_mov_b32_e32 v28, v198
	v_mov_b32_e32 v29, v198
	v_or_b32_e32 v30, 16, v26
	v_pk_fma_f32 v[34:35], v[186:187], s[16:17], v[222:223] op_sel_hi:[1,0,1]
	s_nop 0
	v_med3_f32 v34, v34, s48, v208
	v_med3_f32 v35, v35, s48, v208
	v_pk_mul_f32 v[56:57], v[34:35], s[18:19] op_sel_hi:[1,0]
	v_pk_fma_f32 v[32:33], v[188:189], s[16:17], v[224:225] op_sel_hi:[1,0,1]
	v_exp_f32_e32 v56, v56
	v_exp_f32_e32 v57, v57
	v_pk_fma_f32 v[38:39], v[194:195], s[16:17], v[218:219] op_sel_hi:[1,0,1]
	v_med3_f32 v32, v32, s48, v208
	v_med3_f32 v33, v33, s48, v208
	v_med3_f32 v38, v38, s48, v208
	v_med3_f32 v39, v39, s48, v208
	v_pk_mul_f32 v[58:59], v[32:33], s[18:19] op_sel_hi:[1,0]
	v_pk_mul_f32 v[60:61], v[38:39], s[18:19] op_sel_hi:[1,0]
	v_exp_f32_e32 v58, v58
	v_exp_f32_e32 v59, v59
	v_exp_f32_e32 v60, v60
	v_exp_f32_e32 v61, v61
	v_pk_add_f32 v[56:57], v[56:57], 1.0 op_sel_hi:[1,0]
	v_pk_fma_f32 v[36:37], v[196:197], s[16:17], v[220:221] op_sel_hi:[1,0,1]
	v_mul_f32_e32 v27, v56, v57
	v_med3_f32 v36, v36, s48, v208
	v_med3_f32 v37, v37, s48, v208
	v_pk_fma_f32 v[64:65], v[172:173], s[16:17], v[228:229] op_sel_hi:[1,0,1]
	v_rcp_f32_e32 v172, v27
	v_pk_mul_f32 v[62:63], v[36:37], s[18:19] op_sel_hi:[1,0]
	v_pk_add_f32 v[58:59], v[58:59], 1.0 op_sel_hi:[1,0]
	v_exp_f32_e32 v62, v62
	v_exp_f32_e32 v63, v63
	v_pk_add_f32 v[60:61], v[60:61], 1.0 op_sel_hi:[1,0]
	v_pk_fma_f32 v[50:51], v[174:175], s[16:17], v[226:227] op_sel_hi:[1,0,1]
	v_mul_f32_e32 v31, v58, v59
	v_mul_f32_e32 v173, v60, v61
	v_med3_f32 v50, v50, s49, v208
	v_med3_f32 v51, v51, s49, v208
	v_rcp_f32_e32 v174, v31
	v_pk_mul_f32 v[56:57], v[56:57], v[172:173] op_sel:[1,0] op_sel_hi:[0,0]
	v_pk_add_f32 v[50:51], v[50:51], 1.0 op_sel_hi:[1,0]
	v_pk_mul_f32 v[34:35], v[34:35], v[56:57]
	v_pk_add_f32 v[62:63], v[62:63], 1.0 op_sel_hi:[1,0]
	v_pk_mul_f32 v[34:35], v[50:51], v[34:35]
	v_pk_fma_f32 v[48:49], v[176:177], s[16:17], v[228:229] op_sel_hi:[1,0,1]
	v_mul_f32_e32 v175, v62, v63
	v_cvt_pk_fp8_f32 v28, v34, v35
	v_med3_f32 v48, v48, s49, v208
	v_med3_f32 v49, v49, s49, v208
	v_pk_mul_f32 v[58:59], v[58:59], v[174:175] op_sel:[1,0] op_sel_hi:[0,0]
	v_pk_fma_f32 v[42:43], v[190:191], s[16:17], v[222:223] op_sel_hi:[1,0,1]
	v_pk_add_f32 v[48:49], v[48:49], 1.0 op_sel_hi:[1,0]
	v_rcp_f32_e32 v176, v173
	v_pk_mul_f32 v[32:33], v[32:33], v[58:59]
	v_med3_f32 v42, v42, s48, v208
	v_med3_f32 v43, v43, s48, v208
	v_pk_mul_f32 v[32:33], v[48:49], v[32:33]
	v_pk_fma_f32 v[54:55], v[178:179], s[16:17], v[214:215] op_sel_hi:[1,0,1]
	v_cvt_pk_fp8_f32 v28, v32, v33 op_sel:[0,0,1]
	v_pk_mul_f32 v[32:33], v[42:43], s[18:19] op_sel_hi:[1,0]
	v_rcp_f32_e32 v178, v175
	v_exp_f32_e32 v32, v32
	v_exp_f32_e32 v33, v33
	v_med3_f32 v54, v54, s49, v208
	v_med3_f32 v55, v55, s49, v208
	v_pk_mul_f32 v[60:61], v[60:61], v[176:177] op_sel:[1,0] op_sel_hi:[0,0]
	v_pk_add_f32 v[54:55], v[54:55], 1.0 op_sel_hi:[1,0]
	v_pk_mul_f32 v[38:39], v[38:39], v[60:61]
	v_pk_fma_f32 v[40:41], v[192:193], s[16:17], v[224:225] op_sel_hi:[1,0,1]
	v_pk_fma_f32 v[52:53], v[180:181], s[16:17], v[216:217] op_sel_hi:[1,0,1]
	v_pk_mul_f32 v[38:39], v[54:55], v[38:39]
	v_med3_f32 v52, v52, s49, v208
	v_med3_f32 v53, v53, s49, v208
	v_pk_mul_f32 v[62:63], v[62:63], v[178:179] op_sel:[1,0] op_sel_hi:[0,0]
	v_cvt_pk_fp8_f32 v29, v38, v39
	v_pk_add_f32 v[32:33], v[32:33], 1.0 op_sel_hi:[1,0]
	v_med3_f32 v38, v40, s48, v208
	v_med3_f32 v39, v41, s48, v208
	v_pk_add_f32 v[52:53], v[52:53], 1.0 op_sel_hi:[1,0]
	v_pk_mul_f32 v[36:37], v[36:37], v[62:63]
	v_mul_f32_e32 v27, v32, v33
	v_pk_mul_f32 v[40:41], v[38:39], s[18:19] op_sel_hi:[1,0]
	v_pk_mul_f32 v[34:35], v[52:53], v[36:37]
	v_rcp_f32_e32 v36, v27
	v_exp_f32_e32 v40, v40
	v_exp_f32_e32 v41, v41
	v_pk_fma_f32 v[46:47], v[182:183], s[16:17], v[218:219] op_sel_hi:[1,0,1]
	v_pk_mul_f32 v[32:33], v[32:33], v[36:37] op_sel:[1,0] op_sel_hi:[0,0]
	v_pk_fma_f32 v[170:171], v[170:171], s[16:17], v[226:227] op_sel_hi:[1,0,1]
	v_pk_add_f32 v[36:37], v[40:41], 1.0 op_sel_hi:[1,0]
	v_cvt_pk_fp8_f32 v29, v34, v35 op_sel:[0,0,1]
	v_mul_f32_e32 v27, v36, v37
	v_rcp_f32_e32 v40, v27
	v_med3_f32 v34, v170, s49, v208
	v_med3_f32 v35, v171, s49, v208
	v_pk_add_f32 v[34:35], v[34:35], 1.0 op_sel_hi:[1,0]
	v_pk_mul_f32 v[36:37], v[36:37], v[40:41] op_sel:[1,0] op_sel_hi:[0,0]
	v_pk_mul_f32 v[36:37], v[38:39], v[36:37]
	v_med3_f32 v38, v46, s48, v208
	v_med3_f32 v39, v47, s48, v208
	v_pk_mul_f32 v[40:41], v[38:39], s[18:19] op_sel_hi:[1,0]
	v_pk_mul_f32 v[32:33], v[42:43], v[32:33]
	v_exp_f32_e32 v40, v40
	v_exp_f32_e32 v41, v41
	v_pk_mul_f32 v[32:33], v[34:35], v[32:33]
	v_med3_f32 v34, v64, s49, v208
	v_med3_f32 v35, v65, s49, v208
; __device__ __forceinline__ unsigned pk4_fp8(float a, float b, float c, float d) { int w = __builtin_amdgcn_cvt_pk_fp8_f32(a, b, 0, false); w = __builtin_amdgcn_cvt_pk_fp8_f32(c, d, w, true); return (unsigned)w; }
;     __device__ __forceinline__ void operator()(const f32x4 (&acc)[2][2][4][2], const pg8::Unit& u, int wr, int wc, int fr, int fq) const {
;     ...
;             for (int m = 0; m < 4; ++m) { const int rl = ai * 128 + wr * 64 + m * 16 + fr;
;                 const f32x4 g0 = acc[ai][0][m][0] * (1.0f / 64.0f) + bg0, g1 = acc[ai][0][m][1] * (1.0f / 64.0f) + bg1, u0 = acc[ai][1][m][0] * (1.0f / 64.0f) + bu0, u1 = acc[ai][1][m][1] * (1.0f / 64.0f) + bu1;
;                 const f32x2 h0 = act2((f32x2){g0[0], g0[1]}, (f32x2){u0[0], u0[1]}), h1 = act2((f32x2){g0[2], g0[3]}, (f32x2){u0[2], u0[3]});
;                 const f32x2 h2 = act2((f32x2){g1[0], g1[1]}, (f32x2){u1[0], u1[1]}), h3 = act2((f32x2){g1[2], g1[3]}, (f32x2){u1[2], u1[3]});
;                 *(u32x2*)(Ht + (size_t)rl * FF + hc) = (u32x2){pk4_fp8(h0.x, h0.y, h1.x, h1.y), pk4_fp8(h2.x, h2.y, h3.x, h3.y)}; }
	v_pk_add_f32 v[34:35], v[34:35], 1.0 op_sel_hi:[1,0]
	v_pk_fma_f32 v[44:45], v[184:185], s[16:17], v[220:221] op_sel_hi:[1,0,1]
	v_pk_mul_f32 v[34:35], v[34:35], v[36:37]
	v_pk_add_f32 v[36:37], v[40:41], 1.0 op_sel_hi:[1,0]
	v_med3_f32 v42, v44, s48, v208
	v_mul_f32_e32 v27, v36, v37
	v_med3_f32 v43, v45, s48, v208
	v_rcp_f32_e32 v40, v27
	v_pk_mul_f32 v[44:45], v[42:43], s[18:19] op_sel_hi:[1,0]
	global_store_dwordx2 v[22:23], v[28:29], off
	v_exp_f32_e32 v44, v44
	v_exp_f32_e32 v45, v45
	v_pk_mul_f32 v[36:37], v[36:37], v[40:41] op_sel:[1,0] op_sel_hi:[0,0]
	v_pk_mul_f32 v[36:37], v[38:39], v[36:37]
	v_pk_fma_f32 v[28:29], v[166:167], s[16:17], v[214:215] op_sel_hi:[1,0,1]
	v_pk_add_f32 v[38:39], v[44:45], 1.0 op_sel_hi:[1,0]
	v_med3_f32 v28, v28, s49, v208
	v_mul_f32_e32 v27, v38, v39
	v_rcp_f32_e32 v40, v27
	v_med3_f32 v29, v29, s49, v208
	v_pk_add_f32 v[28:29], v[28:29], 1.0 op_sel_hi:[1,0]
	v_pk_fma_f32 v[168:169], v[168:169], s[16:17], v[216:217] op_sel_hi:[1,0,1]
	v_pk_mul_f32 v[38:39], v[38:39], v[40:41] op_sel:[1,0] op_sel_hi:[0,0]
	v_mov_b32_e32 v40, v198
	v_cvt_pk_fp8_f32 v40, v32, v33
	v_pk_fma_f32 v[32:33], v[154:155], s[16:17], v[222:223] op_sel_hi:[1,0,1]
	v_pk_mul_f32 v[28:29], v[28:29], v[36:37]
	v_med3_f32 v32, v32, s48, v208
	v_med3_f32 v33, v33, s48, v208
	v_mov_b32_e32 v41, v198
	v_pk_mul_f32 v[44:45], v[32:33], s[18:19] op_sel_hi:[1,0]
	v_cvt_pk_fp8_f32 v41, v28, v29
	v_exp_f32_e32 v44, v44
	v_exp_f32_e32 v45, v45
	v_med3_f32 v36, v168, s49, v208
	v_med3_f32 v37, v169, s49, v208
	v_pk_add_f32 v[36:37], v[36:37], 1.0 op_sel_hi:[1,0]
	v_pk_mul_f32 v[28:29], v[42:43], v[38:39]
	v_ashrrev_i32_e32 v31, 31, v30
	v_pk_mul_f32 v[28:29], v[36:37], v[28:29]
	v_pk_add_f32 v[44:45], v[44:45], 1.0 op_sel_hi:[1,0]
	v_cvt_pk_fp8_f32 v41, v28, v29 op_sel:[0,0,1]
	v_lshlrev_b64 v[28:29], 10, v[30:31]
	v_pk_fma_f32 v[30:31], v[156:157], s[16:17], v[224:225] op_sel_hi:[1,0,1]
	v_mul_f32_e32 v27, v44, v45
	v_med3_f32 v30, v30, s48, v208
	v_med3_f32 v31, v31, s48, v208
	v_rcp_f32_e32 v48, v27
	v_pk_mul_f32 v[50:51], v[30:31], s[18:19] op_sel_hi:[1,0]
	v_cvt_pk_fp8_f32 v40, v34, v35 op_sel:[0,0,1]
	v_exp_f32_e32 v50, v50
	v_exp_f32_e32 v51, v51
	v_pk_mul_f32 v[44:45], v[44:45], v[48:49] op_sel:[1,0] op_sel_hi:[0,0]
	v_pk_mul_f32 v[32:33], v[32:33], v[44:45]
	v_lshl_add_u64 v[28:29], v[24:25], 0, v[28:29]
	v_pk_add_f32 v[44:45], v[50:51], 1.0 op_sel_hi:[1,0]
	global_store_dwordx2 v[28:29], v[40:41], off
	v_mul_f32_e32 v27, v44, v45
	v_rcp_f32_e32 v48, v27
	v_pk_fma_f32 v[40:41], v[162:163], s[16:17], v[226:227] op_sel_hi:[1,0,1]
	v_pk_fma_f32 v[36:37], v[150:151], s[16:17], v[218:219] op_sel_hi:[1,0,1]
	v_med3_f32 v40, v40, s49, v208
	v_med3_f32 v41, v41, s49, v208
	v_pk_add_f32 v[40:41], v[40:41], 1.0 op_sel_hi:[1,0]
	v_med3_f32 v36, v36, s48, v208
	v_pk_mul_f32 v[32:33], v[40:41], v[32:33]
	v_pk_mul_f32 v[40:41], v[44:45], v[48:49] op_sel:[1,0] op_sel_hi:[0,0]
	v_med3_f32 v37, v37, s48, v208
	v_pk_mul_f32 v[30:31], v[30:31], v[40:41]
	v_pk_mul_f32 v[40:41], v[36:37], s[18:19] op_sel_hi:[1,0]
	v_pk_fma_f32 v[38:39], v[164:165], s[16:17], v[228:229] op_sel_hi:[1,0,1]
	v_exp_f32_e32 v40, v40
	v_exp_f32_e32 v41, v41
	v_pk_fma_f32 v[34:35], v[152:153], s[16:17], v[220:221] op_sel_hi:[1,0,1]
	v_med3_f32 v38, v38, s49, v208
	v_med3_f32 v39, v39, s49, v208
	v_pk_add_f32 v[40:41], v[40:41], 1.0 op_sel_hi:[1,0]
	v_pk_fma_f32 v[46:47], v[158:159], s[16:17], v[214:215] op_sel_hi:[1,0,1]
	v_pk_add_f32 v[38:39], v[38:39], 1.0 op_sel_hi:[1,0]
	v_mul_f32_e32 v27, v40, v41
	v_med3_f32 v34, v34, s48, v208
	v_med3_f32 v35, v35, s48, v208
	v_pk_mul_f32 v[30:31], v[38:39], v[30:31]
	v_med3_f32 v38, v46, s49, v208
	v_med3_f32 v39, v47, s49, v208
	v_rcp_f32_e32 v44, v27
	v_pk_mul_f32 v[46:47], v[34:35], s[18:19] op_sel_hi:[1,0]
	v_pk_fma_f32 v[42:43], v[160:161], s[16:17], v[216:217] op_sel_hi:[1,0,1]
	v_exp_f32_e32 v46, v46
	v_exp_f32_e32 v47, v47
	v_pk_mul_f32 v[40:41], v[40:41], v[44:45] op_sel:[1,0] op_sel_hi:[0,0]
	v_pk_mul_f32 v[36:37], v[36:37], v[40:41]
	v_pk_add_f32 v[38:39], v[38:39], 1.0 op_sel_hi:[1,0]
	v_pk_add_f32 v[40:41], v[46:47], 1.0 op_sel_hi:[1,0]
	v_pk_mul_f32 v[36:37], v[38:39], v[36:37]
	v_mul_f32_e32 v27, v40, v41
	v_rcp_f32_e32 v44, v27
	v_med3_f32 v38, v42, s49, v208
	v_med3_f32 v39, v43, s49, v208
	v_mov_b32_e32 v42, v198
	v_mov_b32_e32 v43, v198
	v_cvt_pk_fp8_f32 v42, v32, v33
	v_cvt_pk_fp8_f32 v43, v36, v37
	v_pk_mul_f32 v[40:41], v[40:41], v[44:45] op_sel:[1,0] op_sel_hi:[0,0]
	v_pk_add_f32 v[38:39], v[38:39], 1.0 op_sel_hi:[1,0]
	v_pk_mul_f32 v[32:33], v[34:35], v[40:41]
	v_or_b32_e32 v28, 32, v26
	v_pk_mul_f32 v[32:33], v[38:39], v[32:33]
	v_cvt_pk_fp8_f32 v42, v30, v31 op_sel:[0,0,1]
	v_cvt_pk_fp8_f32 v43, v32, v33 op_sel:[0,0,1]
	v_ashrrev_i32_e32 v29, 31, v28
	v_lshlrev_b64 v[28:29], 10, v[28:29]
	v_pk_fma_f32 v[30:31], v[138:139], s[16:17], v[222:223] op_sel_hi:[1,0,1]
	v_lshl_add_u64 v[28:29], v[24:25], 0, v[28:29]
	v_med3_f32 v30, v30, s48, v208
	v_med3_f32 v31, v31, s48, v208
	global_store_dwordx2 v[28:29], v[42:43], off
	v_pk_mul_f32 v[42:43], v[30:31], s[18:19] op_sel_hi:[1,0]
	v_pk_fma_f32 v[28:29], v[140:141], s[16:17], v[224:225] op_sel_hi:[1,0,1]
	v_exp_f32_e32 v42, v42
	v_exp_f32_e32 v43, v43
	v_med3_f32 v28, v28, s48, v208
	v_med3_f32 v29, v29, s48, v208
	v_pk_mul_f32 v[48:49], v[28:29], s[18:19] op_sel_hi:[1,0]
	v_pk_add_f32 v[42:43], v[42:43], 1.0 op_sel_hi:[1,0]
	v_exp_f32_e32 v48, v48
	v_mul_f32_e32 v27, v42, v43
	v_rcp_f32_e32 v46, v27
	v_exp_f32_e32 v49, v49
	v_pk_fma_f32 v[38:39], v[146:147], s[16:17], v[226:227] op_sel_hi:[1,0,1]
	v_pk_fma_f32 v[34:35], v[134:135], s[16:17], v[218:219] op_sel_hi:[1,0,1]
; __device__ __forceinline__ unsigned pk4_fp8(float a, float b, float c, float d) { int w = __builtin_amdgcn_cvt_pk_fp8_f32(a, b, 0, false); w = __builtin_amdgcn_cvt_pk_fp8_f32(c, d, w, true); return (unsigned)w; }
;     __device__ __forceinline__ void operator()(const f32x4 (&acc)[2][2][4][2], const pg8::Unit& u, int wr, int wc, int fr, int fq) const {
;     ...
;             for (int m = 0; m < 4; ++m) { const int rl = ai * 128 + wr * 64 + m * 16 + fr;
;                 const f32x4 g0 = acc[ai][0][m][0] * (1.0f / 64.0f) + bg0, g1 = acc[ai][0][m][1] * (1.0f / 64.0f) + bg1, u0 = acc[ai][1][m][0] * (1.0f / 64.0f) + bu0, u1 = acc[ai][1][m][1] * (1.0f / 64.0f) + bu1;
;                 const f32x2 h0 = act2((f32x2){g0[0], g0[1]}, (f32x2){u0[0], u0[1]}), h1 = act2((f32x2){g0[2], g0[3]}, (f32x2){u0[2], u0[3]});
;                 const f32x2 h2 = act2((f32x2){g1[0], g1[1]}, (f32x2){u1[0], u1[1]}), h3 = act2((f32x2){g1[2], g1[3]}, (f32x2){u1[2], u1[3]});
;                 *(u32x2*)(Ht + (size_t)rl * FF + hc) = (u32x2){pk4_fp8(h0.x, h0.y, h1.x, h1.y), pk4_fp8(h2.x, h2.y, h3.x, h3.y)}; }
	v_pk_mul_f32 v[42:43], v[42:43], v[46:47] op_sel:[1,0] op_sel_hi:[0,0]
	v_pk_mul_f32 v[30:31], v[30:31], v[42:43]
	v_pk_add_f32 v[42:43], v[48:49], 1.0 op_sel_hi:[1,0]
	v_med3_f32 v38, v38, s49, v208
	v_mul_f32_e32 v27, v42, v43
	v_rcp_f32_e32 v46, v27
	v_med3_f32 v39, v39, s49, v208
	v_pk_add_f32 v[38:39], v[38:39], 1.0 op_sel_hi:[1,0]
	v_med3_f32 v34, v34, s48, v208
	v_pk_mul_f32 v[30:31], v[38:39], v[30:31]
	v_pk_mul_f32 v[38:39], v[42:43], v[46:47] op_sel:[1,0] op_sel_hi:[0,0]
	v_med3_f32 v35, v35, s48, v208
	v_pk_mul_f32 v[28:29], v[28:29], v[38:39]
	v_pk_mul_f32 v[38:39], v[34:35], s[18:19] op_sel_hi:[1,0]
	v_pk_fma_f32 v[36:37], v[148:149], s[16:17], v[228:229] op_sel_hi:[1,0,1]
	v_exp_f32_e32 v38, v38
	v_exp_f32_e32 v39, v39
	v_pk_fma_f32 v[32:33], v[136:137], s[16:17], v[220:221] op_sel_hi:[1,0,1]
	v_med3_f32 v36, v36, s49, v208
	v_med3_f32 v37, v37, s49, v208
	v_pk_add_f32 v[38:39], v[38:39], 1.0 op_sel_hi:[1,0]
	v_pk_fma_f32 v[44:45], v[142:143], s[16:17], v[214:215] op_sel_hi:[1,0,1]
	v_pk_add_f32 v[36:37], v[36:37], 1.0 op_sel_hi:[1,0]
	v_mul_f32_e32 v27, v38, v39
	v_med3_f32 v32, v32, s48, v208
	v_med3_f32 v33, v33, s48, v208
	v_pk_mul_f32 v[28:29], v[36:37], v[28:29]
	v_med3_f32 v36, v44, s49, v208
	v_med3_f32 v37, v45, s49, v208
	v_rcp_f32_e32 v42, v27
	v_pk_mul_f32 v[44:45], v[32:33], s[18:19] op_sel_hi:[1,0]
	v_or_b32_e32 v26, 48, v26
	v_exp_f32_e32 v44, v44
	v_exp_f32_e32 v45, v45
	v_pk_mul_f32 v[38:39], v[38:39], v[42:43] op_sel:[1,0] op_sel_hi:[0,0]
	v_pk_mul_f32 v[34:35], v[34:35], v[38:39]
	v_pk_fma_f32 v[40:41], v[144:145], s[16:17], v[216:217] op_sel_hi:[1,0,1]
	v_pk_add_f32 v[38:39], v[44:45], 1.0 op_sel_hi:[1,0]
	v_pk_add_f32 v[36:37], v[36:37], 1.0 op_sel_hi:[1,0]
	v_mul_f32_e32 v27, v38, v39
	v_rcp_f32_e32 v42, v27
	v_pk_mul_f32 v[34:35], v[36:37], v[34:35]
	v_med3_f32 v36, v40, s49, v208
	v_med3_f32 v37, v41, s49, v208
	v_mov_b32_e32 v40, v198
	v_mov_b32_e32 v41, v198
	v_ashrrev_i32_e32 v27, 31, v26
	v_cvt_pk_fp8_f32 v40, v30, v31
	v_cvt_pk_fp8_f32 v41, v34, v35
	v_lshlrev_b64 v[26:27], 10, v[26:27]
	v_pk_mul_f32 v[38:39], v[38:39], v[42:43] op_sel:[1,0] op_sel_hi:[0,0]
	v_lshl_add_u64 v[24:25], v[24:25], 0, v[26:27]
	v_pk_fma_f32 v[26:27], v[122:123], s[16:17], v[222:223] op_sel_hi:[1,0,1]
	v_pk_add_f32 v[36:37], v[36:37], 1.0 op_sel_hi:[1,0]
	v_pk_mul_f32 v[30:31], v[32:33], v[38:39]
	v_med3_f32 v26, v26, s48, v208
	v_med3_f32 v27, v27, s48, v208
	v_pk_mul_f32 v[30:31], v[36:37], v[30:31]
	v_pk_mul_f32 v[38:39], v[26:27], s[18:19] op_sel_hi:[1,0]
	v_cvt_pk_fp8_f32 v40, v28, v29 op_sel:[0,0,1]
	v_cvt_pk_fp8_f32 v41, v30, v31 op_sel:[0,0,1]
	v_exp_f32_e32 v38, v38
	v_exp_f32_e32 v39, v39
	v_pk_fma_f32 v[34:35], v[130:131], s[16:17], v[226:227] op_sel_hi:[1,0,1]
	global_store_dwordx2 v[24:25], v[40:41], off
	v_pk_fma_f32 v[24:25], v[124:125], s[16:17], v[224:225] op_sel_hi:[1,0,1]
	v_pk_add_f32 v[38:39], v[38:39], 1.0 op_sel_hi:[1,0]
	v_med3_f32 v24, v24, s48, v208
	v_mul_f32_e32 v42, v38, v39
	v_med3_f32 v25, v25, s48, v208
	v_rcp_f32_e32 v42, v42
	v_pk_mul_f32 v[44:45], v[24:25], s[18:19] op_sel_hi:[1,0]
	v_med3_f32 v34, v34, s49, v208
	v_exp_f32_e32 v44, v44
	v_exp_f32_e32 v45, v45
	v_pk_mul_f32 v[38:39], v[38:39], v[42:43] op_sel:[1,0] op_sel_hi:[0,0]
	v_pk_mul_f32 v[26:27], v[26:27], v[38:39]
	v_med3_f32 v35, v35, s49, v208
	v_pk_add_f32 v[38:39], v[44:45], 1.0 op_sel_hi:[1,0]
	v_pk_fma_f32 v[30:31], v[118:119], s[16:17], v[218:219] op_sel_hi:[1,0,1]
	v_mul_f32_e32 v42, v38, v39
	v_rcp_f32_e32 v42, v42
	v_pk_add_f32 v[34:35], v[34:35], 1.0 op_sel_hi:[1,0]
	v_med3_f32 v30, v30, s48, v208
	v_pk_mul_f32 v[26:27], v[34:35], v[26:27]
	v_pk_mul_f32 v[34:35], v[38:39], v[42:43] op_sel:[1,0] op_sel_hi:[0,0]
	v_med3_f32 v31, v31, s48, v208
	v_pk_mul_f32 v[24:25], v[24:25], v[34:35]
	v_pk_mul_f32 v[34:35], v[30:31], s[18:19] op_sel_hi:[1,0]
	v_pk_fma_f32 v[32:33], v[132:133], s[16:17], v[228:229] op_sel_hi:[1,0,1]
	v_exp_f32_e32 v34, v34
	v_exp_f32_e32 v35, v35
	v_pk_fma_f32 v[28:29], v[120:121], s[16:17], v[220:221] op_sel_hi:[1,0,1]
	v_med3_f32 v32, v32, s49, v208
	v_med3_f32 v33, v33, s49, v208
	v_pk_add_f32 v[34:35], v[34:35], 1.0 op_sel_hi:[1,0]
	v_pk_fma_f32 v[40:41], v[126:127], s[16:17], v[214:215] op_sel_hi:[1,0,1]
	v_pk_add_f32 v[32:33], v[32:33], 1.0 op_sel_hi:[1,0]
	v_mul_f32_e32 v38, v34, v35
	v_med3_f32 v28, v28, s48, v208
	v_med3_f32 v29, v29, s48, v208
	v_pk_mul_f32 v[24:25], v[32:33], v[24:25]
	v_med3_f32 v32, v40, s49, v208
	v_med3_f32 v33, v41, s49, v208
	v_rcp_f32_e32 v38, v38
	v_pk_mul_f32 v[40:41], v[28:29], s[18:19] op_sel_hi:[1,0]
	v_pk_fma_f32 v[36:37], v[128:129], s[16:17], v[216:217] op_sel_hi:[1,0,1]
	v_exp_f32_e32 v40, v40
	v_exp_f32_e32 v41, v41
	v_pk_mul_f32 v[34:35], v[34:35], v[38:39] op_sel:[1,0] op_sel_hi:[0,0]
	v_pk_mul_f32 v[30:31], v[30:31], v[34:35]
	v_pk_add_f32 v[32:33], v[32:33], 1.0 op_sel_hi:[1,0]
	v_pk_add_f32 v[34:35], v[40:41], 1.0 op_sel_hi:[1,0]
	v_pk_mul_f32 v[30:31], v[32:33], v[30:31]
	v_mul_f32_e32 v38, v34, v35
	v_rcp_f32_e32 v38, v38
	v_med3_f32 v33, v37, s49, v208
	v_mov_b32_e32 v37, v198
	v_cvt_pk_fp8_f32 v37, v30, v31
	v_med3_f32 v32, v36, s49, v208
	v_pk_mul_f32 v[34:35], v[34:35], v[38:39] op_sel:[1,0] op_sel_hi:[0,0]
	v_mov_b32_e32 v36, v198
	v_pk_add_f32 v[32:33], v[32:33], 1.0 op_sel_hi:[1,0]
	v_cvt_pk_fp8_f32 v36, v26, v27
	v_pk_mul_f32 v[26:27], v[28:29], v[34:35]
	v_pk_fma_f32 v[34:35], v[114:115], s[16:17], v[226:227] op_sel_hi:[1,0,1]
	v_pk_mul_f32 v[26:27], v[32:33], v[26:27]
	v_cvt_pk_fp8_f32 v36, v24, v25 op_sel:[0,0,1]
	v_cvt_pk_fp8_f32 v37, v26, v27 op_sel:[0,0,1]
	v_pk_fma_f32 v[26:27], v[106:107], s[16:17], v[222:223] op_sel_hi:[1,0,1]
; __device__ __forceinline__ unsigned pk4_fp8(float a, float b, float c, float d) { int w = __builtin_amdgcn_cvt_pk_fp8_f32(a, b, 0, false); w = __builtin_amdgcn_cvt_pk_fp8_f32(c, d, w, true); return (unsigned)w; }
;     __device__ __forceinline__ void operator()(const f32x4 (&acc)[2][2][4][2], const pg8::Unit& u, int wr, int wc, int fr, int fq) const {
;     ...
;             for (int m = 0; m < 4; ++m) { const int rl = ai * 128 + wr * 64 + m * 16 + fr;
;                 const f32x4 g0 = acc[ai][0][m][0] * (1.0f / 64.0f) + bg0, g1 = acc[ai][0][m][1] * (1.0f / 64.0f) + bg1, u0 = acc[ai][1][m][0] * (1.0f / 64.0f) + bu0, u1 = acc[ai][1][m][1] * (1.0f / 64.0f) + bu1;
;                 const f32x2 h0 = act2((f32x2){g0[0], g0[1]}, (f32x2){u0[0], u0[1]}), h1 = act2((f32x2){g0[2], g0[3]}, (f32x2){u0[2], u0[3]});
;                 const f32x2 h2 = act2((f32x2){g1[0], g1[1]}, (f32x2){u1[0], u1[1]}), h3 = act2((f32x2){g1[2], g1[3]}, (f32x2){u1[2], u1[3]});
;                 *(u32x2*)(Ht + (size_t)rl * FF + hc) = (u32x2){pk4_fp8(h0.x, h0.y, h1.x, h1.y), pk4_fp8(h2.x, h2.y, h3.x, h3.y)}; }
	v_add_co_u32_e32 v24, vcc, s50, v22
	v_med3_f32 v26, v26, s48, v208
	v_med3_f32 v27, v27, s48, v208
	v_pk_mul_f32 v[38:39], v[26:27], s[18:19] op_sel_hi:[1,0]
	v_addc_co_u32_e32 v25, vcc, 0, v23, vcc
	v_exp_f32_e32 v38, v38
	v_exp_f32_e32 v39, v39
	global_store_dwordx2 v[24:25], v[36:37], off
	v_pk_fma_f32 v[24:25], v[108:109], s[16:17], v[224:225] op_sel_hi:[1,0,1]
	v_med3_f32 v34, v34, s49, v208
	v_pk_add_f32 v[38:39], v[38:39], 1.0 op_sel_hi:[1,0]
	v_med3_f32 v24, v24, s48, v208
	v_mul_f32_e32 v42, v38, v39
	v_med3_f32 v25, v25, s48, v208
	v_rcp_f32_e32 v42, v42
	v_pk_mul_f32 v[44:45], v[24:25], s[18:19] op_sel_hi:[1,0]
	v_med3_f32 v35, v35, s49, v208
	v_exp_f32_e32 v44, v44
	v_exp_f32_e32 v45, v45
	v_pk_mul_f32 v[38:39], v[38:39], v[42:43] op_sel:[1,0] op_sel_hi:[0,0]
	v_pk_mul_f32 v[26:27], v[26:27], v[38:39]
	v_pk_fma_f32 v[30:31], v[102:103], s[16:17], v[218:219] op_sel_hi:[1,0,1]
	v_pk_add_f32 v[38:39], v[44:45], 1.0 op_sel_hi:[1,0]
	v_pk_add_f32 v[34:35], v[34:35], 1.0 op_sel_hi:[1,0]
	v_mul_f32_e32 v42, v38, v39
	v_rcp_f32_e32 v42, v42
	v_pk_mul_f32 v[26:27], v[34:35], v[26:27]
	v_med3_f32 v30, v30, s48, v208
	v_med3_f32 v31, v31, s48, v208
	v_pk_mul_f32 v[34:35], v[38:39], v[42:43] op_sel:[1,0] op_sel_hi:[0,0]
	v_pk_mul_f32 v[24:25], v[24:25], v[34:35]
	v_pk_mul_f32 v[34:35], v[30:31], s[18:19] op_sel_hi:[1,0]
	v_pk_fma_f32 v[32:33], v[116:117], s[16:17], v[228:229] op_sel_hi:[1,0,1]
	v_exp_f32_e32 v34, v34
	v_exp_f32_e32 v35, v35
	v_pk_fma_f32 v[28:29], v[104:105], s[16:17], v[220:221] op_sel_hi:[1,0,1]
	v_med3_f32 v32, v32, s49, v208
	v_med3_f32 v33, v33, s49, v208
	v_pk_add_f32 v[34:35], v[34:35], 1.0 op_sel_hi:[1,0]
	v_pk_fma_f32 v[40:41], v[110:111], s[16:17], v[214:215] op_sel_hi:[1,0,1]
	v_pk_add_f32 v[32:33], v[32:33], 1.0 op_sel_hi:[1,0]
	v_mul_f32_e32 v38, v34, v35
	v_med3_f32 v28, v28, s48, v208
	v_med3_f32 v29, v29, s48, v208
	v_pk_mul_f32 v[24:25], v[32:33], v[24:25]
	v_med3_f32 v32, v40, s49, v208
	v_med3_f32 v33, v41, s49, v208
	v_rcp_f32_e32 v38, v38
	v_pk_mul_f32 v[40:41], v[28:29], s[18:19] op_sel_hi:[1,0]
	v_pk_fma_f32 v[36:37], v[112:113], s[16:17], v[216:217] op_sel_hi:[1,0,1]
	v_exp_f32_e32 v40, v40
	v_exp_f32_e32 v41, v41
	v_pk_mul_f32 v[34:35], v[34:35], v[38:39] op_sel:[1,0] op_sel_hi:[0,0]
	v_pk_mul_f32 v[30:31], v[30:31], v[34:35]
	v_pk_add_f32 v[32:33], v[32:33], 1.0 op_sel_hi:[1,0]
	v_pk_add_f32 v[34:35], v[40:41], 1.0 op_sel_hi:[1,0]
	v_pk_mul_f32 v[30:31], v[32:33], v[30:31]
	v_mul_f32_e32 v38, v34, v35
	v_rcp_f32_e32 v38, v38
	v_med3_f32 v33, v37, s49, v208
	v_mov_b32_e32 v37, v198
	v_cvt_pk_fp8_f32 v37, v30, v31
	v_med3_f32 v32, v36, s49, v208
	v_pk_mul_f32 v[34:35], v[34:35], v[38:39] op_sel:[1,0] op_sel_hi:[0,0]
	v_mov_b32_e32 v36, v198
	v_pk_add_f32 v[32:33], v[32:33], 1.0 op_sel_hi:[1,0]
	v_cvt_pk_fp8_f32 v36, v26, v27
	v_pk_mul_f32 v[26:27], v[28:29], v[34:35]
	v_pk_fma_f32 v[34:35], v[98:99], s[16:17], v[226:227] op_sel_hi:[1,0,1]
	v_pk_mul_f32 v[26:27], v[32:33], v[26:27]
	v_cvt_pk_fp8_f32 v36, v24, v25 op_sel:[0,0,1]
	v_cvt_pk_fp8_f32 v37, v26, v27 op_sel:[0,0,1]
	v_pk_fma_f32 v[26:27], v[90:91], s[16:17], v[222:223] op_sel_hi:[1,0,1]
	v_add_co_u32_e32 v24, vcc, s51, v22
	v_med3_f32 v26, v26, s48, v208
	v_med3_f32 v27, v27, s48, v208
	v_pk_mul_f32 v[38:39], v[26:27], s[18:19] op_sel_hi:[1,0]
	v_addc_co_u32_e32 v25, vcc, 0, v23, vcc
	v_exp_f32_e32 v38, v38
	v_exp_f32_e32 v39, v39
	global_store_dwordx2 v[24:25], v[36:37], off
	v_pk_fma_f32 v[24:25], v[92:93], s[16:17], v[224:225] op_sel_hi:[1,0,1]
	v_med3_f32 v34, v34, s49, v208
	v_pk_add_f32 v[38:39], v[38:39], 1.0 op_sel_hi:[1,0]
	v_med3_f32 v24, v24, s48, v208
	v_mul_f32_e32 v42, v38, v39
	v_med3_f32 v25, v25, s48, v208
	v_rcp_f32_e32 v42, v42
	v_pk_mul_f32 v[44:45], v[24:25], s[18:19] op_sel_hi:[1,0]
	v_med3_f32 v35, v35, s49, v208
	v_exp_f32_e32 v44, v44
	v_exp_f32_e32 v45, v45
	v_pk_mul_f32 v[38:39], v[38:39], v[42:43] op_sel:[1,0] op_sel_hi:[0,0]
	v_pk_mul_f32 v[26:27], v[26:27], v[38:39]
	v_pk_fma_f32 v[30:31], v[86:87], s[16:17], v[218:219] op_sel_hi:[1,0,1]
	v_pk_add_f32 v[38:39], v[44:45], 1.0 op_sel_hi:[1,0]
	v_pk_add_f32 v[34:35], v[34:35], 1.0 op_sel_hi:[1,0]
	v_mul_f32_e32 v42, v38, v39
	v_rcp_f32_e32 v42, v42
	v_pk_mul_f32 v[26:27], v[34:35], v[26:27]
	v_med3_f32 v30, v30, s48, v208
	v_med3_f32 v31, v31, s48, v208
	v_pk_mul_f32 v[34:35], v[38:39], v[42:43] op_sel:[1,0] op_sel_hi:[0,0]
	v_pk_mul_f32 v[24:25], v[24:25], v[34:35]
	v_pk_mul_f32 v[34:35], v[30:31], s[18:19] op_sel_hi:[1,0]
	v_pk_fma_f32 v[32:33], v[100:101], s[16:17], v[228:229] op_sel_hi:[1,0,1]
	v_exp_f32_e32 v34, v34
	v_exp_f32_e32 v35, v35
	v_pk_fma_f32 v[28:29], v[88:89], s[16:17], v[220:221] op_sel_hi:[1,0,1]
	v_med3_f32 v32, v32, s49, v208
	v_med3_f32 v33, v33, s49, v208
	v_pk_add_f32 v[34:35], v[34:35], 1.0 op_sel_hi:[1,0]
	v_pk_fma_f32 v[40:41], v[94:95], s[16:17], v[214:215] op_sel_hi:[1,0,1]
; __device__ __forceinline__ unsigned pk4_fp8(float a, float b, float c, float d) { int w = __builtin_amdgcn_cvt_pk_fp8_f32(a, b, 0, false); w = __builtin_amdgcn_cvt_pk_fp8_f32(c, d, w, true); return (unsigned)w; }
; #define PG8_UNI64(p) ((const char*)((((unsigned long long)(unsigned)__builtin_amdgcn_readfirstlane((int)((unsigned long long)(p) >> 32))) << 32) | (unsigned long long)(unsigned)__builtin_amdgcn_readfirstlane((int)(unsigned)(unsigned long long)(p))))
;     __device__ __forceinline__ const char* Abase(const pg8::Unit& u) const { size_t o = WS_R1; if (u.aux == 1) o = WS_R3; return ws + o + (size_t)u.pm * TSF8; }
;     __device__ __forceinline__ const char* Bbase(const pg8::Unit& u) const { size_t o = WS_WIN; if (u.aux == 1) o = WS_WKV; return ws + o + (size_t)u.pn * TSF8; }
;     __device__ __forceinline__ const char* Abase(const pg8::Unit& u) const { if (GATH) return ws + WS_XQ; return ws + WS_H2 + (size_t)u.pm * TSF8; }
; template <class Epi, class Sched, bool F8 = false, bool PF = false, bool I8 = false, int PID = -1>
; __device__ __forceinline__ void gemm_phase(LAS unsigned char* lds, LAS unsigned char* xlds, const int RP, const int RPB, const int nt, const Sched& S, const Epi& E, const int stagger_ticks) {
;     ...
;         cur = nxt; cA = nA; cB = nB; ++ui;
;         has_next = has_nn; nxt = nn;
;         if (has_next) { nA = PG8_UNI64(S.Abase(nxt)); nB = PG8_UNI64(S.Bbase(nxt)); }
;     __device__ __forceinline__ void operator()(const f32x4 (&acc)[2][2][4][2], const pg8::Unit& u, int wr, int wc, int fr, int fq) const {
;     ...
;             for (int m = 0; m < 4; ++m) { const int rl = ai * 128 + wr * 64 + m * 16 + fr;
;                 const f32x4 g0 = acc[ai][0][m][0] * (1.0f / 64.0f) + bg0, g1 = acc[ai][0][m][1] * (1.0f / 64.0f) + bg1, u0 = acc[ai][1][m][0] * (1.0f / 64.0f) + bu0, u1 = acc[ai][1][m][1] * (1.0f / 64.0f) + bu1;
;                 const f32x2 h0 = act2((f32x2){g0[0], g0[1]}, (f32x2){u0[0], u0[1]}), h1 = act2((f32x2){g0[2], g0[3]}, (f32x2){u0[2], u0[3]});
;                 const f32x2 h2 = act2((f32x2){g1[0], g1[1]}, (f32x2){u1[0], u1[1]}), h3 = act2((f32x2){g1[2], g1[3]}, (f32x2){u1[2], u1[3]});
;                 *(u32x2*)(Ht + (size_t)rl * FF + hc) = (u32x2){pk4_fp8(h0.x, h0.y, h1.x, h1.y), pk4_fp8(h2.x, h2.y, h3.x, h3.y)}; }
	v_pk_add_f32 v[32:33], v[32:33], 1.0 op_sel_hi:[1,0]
	v_mul_f32_e32 v38, v34, v35
	v_med3_f32 v28, v28, s48, v208
	v_med3_f32 v29, v29, s48, v208
	v_pk_mul_f32 v[24:25], v[32:33], v[24:25]
	v_med3_f32 v32, v40, s49, v208
	v_med3_f32 v33, v41, s49, v208
	v_rcp_f32_e32 v38, v38
	v_pk_mul_f32 v[40:41], v[28:29], s[18:19] op_sel_hi:[1,0]
	v_pk_fma_f32 v[36:37], v[96:97], s[16:17], v[216:217] op_sel_hi:[1,0,1]
	v_exp_f32_e32 v40, v40
	v_exp_f32_e32 v41, v41
	v_pk_mul_f32 v[34:35], v[34:35], v[38:39] op_sel:[1,0] op_sel_hi:[0,0]
	v_pk_mul_f32 v[30:31], v[30:31], v[34:35]
	v_pk_add_f32 v[32:33], v[32:33], 1.0 op_sel_hi:[1,0]
	v_pk_add_f32 v[34:35], v[40:41], 1.0 op_sel_hi:[1,0]
	v_pk_mul_f32 v[30:31], v[32:33], v[30:31]
	v_mul_f32_e32 v38, v34, v35
	v_rcp_f32_e32 v38, v38
	v_med3_f32 v32, v36, s49, v208
	v_med3_f32 v33, v37, s49, v208
	v_mov_b32_e32 v36, v198
	v_mov_b32_e32 v37, v198
	v_cvt_pk_fp8_f32 v36, v26, v27
	v_cvt_pk_fp8_f32 v37, v30, v31
	v_pk_mul_f32 v[34:35], v[34:35], v[38:39] op_sel:[1,0] op_sel_hi:[0,0]
	v_pk_add_f32 v[32:33], v[32:33], 1.0 op_sel_hi:[1,0]
	v_pk_mul_f32 v[26:27], v[28:29], v[34:35]
	v_cvt_pk_fp8_f32 v36, v24, v25 op_sel:[0,0,1]
	v_pk_mul_f32 v[26:27], v[32:33], v[26:27]
	v_add_co_u32_e32 v24, vcc, s60, v22
	v_cvt_pk_fp8_f32 v37, v26, v27 op_sel:[0,0,1]
	v_pk_fma_f32 v[14:15], v[74:75], s[16:17], v[222:223] op_sel_hi:[1,0,1]
	v_addc_co_u32_e32 v25, vcc, 0, v23, vcc
	v_med3_f32 v14, v14, s48, v208
	v_med3_f32 v15, v15, s48, v208
	global_store_dwordx2 v[24:25], v[36:37], off
	v_pk_mul_f32 v[24:25], v[14:15], s[18:19] op_sel_hi:[1,0]
	v_pk_fma_f32 v[16:17], v[76:77], s[16:17], v[224:225] op_sel_hi:[1,0,1]
	v_exp_f32_e32 v24, v24
	v_exp_f32_e32 v25, v25
	v_med3_f32 v16, v16, s48, v208
	v_med3_f32 v17, v17, s48, v208
	v_pk_mul_f32 v[28:29], v[16:17], s[18:19] op_sel_hi:[1,0]
	v_pk_add_f32 v[24:25], v[24:25], 1.0 op_sel_hi:[1,0]
	v_exp_f32_e32 v28, v28
	v_mul_f32_e32 v26, v24, v25
	v_rcp_f32_e32 v26, v26
	v_exp_f32_e32 v29, v29
	v_pk_fma_f32 v[18:19], v[82:83], s[16:17], v[226:227] op_sel_hi:[1,0,1]
	v_pk_fma_f32 v[10:11], v[70:71], s[16:17], v[218:219] op_sel_hi:[1,0,1]
	v_pk_mul_f32 v[24:25], v[24:25], v[26:27] op_sel:[1,0] op_sel_hi:[0,0]
	v_pk_mul_f32 v[14:15], v[14:15], v[24:25]
	v_pk_add_f32 v[24:25], v[28:29], 1.0 op_sel_hi:[1,0]
	v_med3_f32 v18, v18, s49, v208
	v_mul_f32_e32 v26, v24, v25
	v_rcp_f32_e32 v26, v26
	v_med3_f32 v19, v19, s49, v208
	v_pk_fma_f32 v[20:21], v[84:85], s[16:17], v[228:229] op_sel_hi:[1,0,1]
	v_pk_add_f32 v[18:19], v[18:19], 1.0 op_sel_hi:[1,0]
	v_med3_f32 v10, v10, s48, v208
	v_pk_mul_f32 v[14:15], v[18:19], v[14:15]
	v_med3_f32 v18, v20, s49, v208
	v_med3_f32 v19, v21, s49, v208
	v_pk_mul_f32 v[20:21], v[24:25], v[26:27] op_sel:[1,0] op_sel_hi:[0,0]
	v_med3_f32 v11, v11, s48, v208
	v_pk_mul_f32 v[16:17], v[16:17], v[20:21]
	v_pk_mul_f32 v[20:21], v[10:11], s[18:19] op_sel_hi:[1,0]
	v_pk_add_f32 v[18:19], v[18:19], 1.0 op_sel_hi:[1,0]
	v_exp_f32_e32 v20, v20
	v_exp_f32_e32 v21, v21
	v_pk_fma_f32 v[12:13], v[72:73], s[16:17], v[220:221] op_sel_hi:[1,0,1]
	v_pk_mul_f32 v[16:17], v[18:19], v[16:17]
	v_med3_f32 v12, v12, s48, v208
	v_pk_add_f32 v[18:19], v[20:21], 1.0 op_sel_hi:[1,0]
	v_med3_f32 v13, v13, s48, v208
	v_mul_f32_e32 v20, v18, v19
	v_rcp_f32_e32 v20, v20
	v_pk_mul_f32 v[24:25], v[12:13], s[18:19] op_sel_hi:[1,0]
	v_pk_fma_f32 v[6:7], v[78:79], s[16:17], v[214:215] op_sel_hi:[1,0,1]
	v_exp_f32_e32 v24, v24
	v_exp_f32_e32 v25, v25
	v_pk_mul_f32 v[18:19], v[18:19], v[20:21] op_sel:[1,0] op_sel_hi:[0,0]
	v_pk_mul_f32 v[10:11], v[10:11], v[18:19]
	v_med3_f32 v6, v6, s49, v208
	v_pk_add_f32 v[18:19], v[24:25], 1.0 op_sel_hi:[1,0]
	v_med3_f32 v7, v7, s49, v208
	v_mul_f32_e32 v20, v18, v19
	v_rcp_f32_e32 v20, v20
	v_pk_add_f32 v[6:7], v[6:7], 1.0 op_sel_hi:[1,0]
	v_pk_fma_f32 v[8:9], v[80:81], s[16:17], v[216:217] op_sel_hi:[1,0,1]
	v_pk_mul_f32 v[6:7], v[6:7], v[10:11]
	v_pk_mul_f32 v[10:11], v[18:19], v[20:21] op_sel:[1,0] op_sel_hi:[0,0]
	v_mov_b32_e32 v18, v198
	v_mov_b32_e32 v19, v198
	v_cvt_pk_fp8_f32 v18, v14, v15
	v_cvt_pk_fp8_f32 v19, v6, v7
	v_med3_f32 v8, v8, s49, v208
	v_med3_f32 v9, v9, s49, v208
	v_pk_add_f32 v[8:9], v[8:9], 1.0 op_sel_hi:[1,0]
	v_pk_mul_f32 v[6:7], v[12:13], v[10:11]
	v_cvt_pk_fp8_f32 v18, v16, v17 op_sel:[0,0,1]
	v_pk_mul_f32 v[6:7], v[8:9], v[6:7]
	s_nop 0
	v_cvt_pk_fp8_f32 v19, v6, v7 op_sel:[0,0,1]
	v_add_co_u32_e32 v6, vcc, 0x2c000, v22
	s_nop 1
	v_addc_co_u32_e32 v7, vcc, 0, v23, vcc
	s_and_b64 vcc, exec, s[2:3]
	s_mov_b64 s[2:3], -1
	global_store_dwordx2 v[6:7], v[18:19], off
	s_cbranch_vccnz .LBB0_956
	s_andn2_b64 vcc, exec, s[10:11]
	s_mov_b64 s[22:23], s[8:9]
	s_mov_b64 s[24:25], s[20:21]
	s_cbranch_vccnz .LBB0_972
	s_lshl_b32 s2, s41, 3
	s_add_i32 s2, s2, s39
	s_ashr_i32 s3, s2, 31
	s_lshl_b64 s[2:3], s[2:3], 18
	s_add_u32 s22, s37, s2
	s_addc_u32 s23, s38, s3
	s_mov_b64 s[24:25], s[6:7]
